# GLA: q/k/log-decay bf16 elements loaded with global_load_short_d16_hi into zero-low registers (arrive as f32 bit patterns); 24 per-chunk shift unpacks removed
# speedup vs baseline: 1.0036x; 1.0030x over previous
.LBB0_463:
	s_andn2_b64 vcc, exec, s[0:1]
	s_cbranch_vccnz .LBB0_748
	v_writelane_b32 v255, s86, 39
	s_movk_i32 s1, 0x800
	s_cmpk_gt_i32 s20, 0xff
	v_writelane_b32 v255, s87, 40
	v_writelane_b32 v255, s82, 43
	v_writelane_b32 v255, s94, 44
	s_cbranch_scc1 .LBB0_493
	s_add_u32 s78, s76, 0x46600000
	s_addc_u32 s79, s77, 0
	s_add_u32 s80, s76, 0x15e00000
	s_addc_u32 s81, s77, 0
	s_lshl_b32 s82, s71, 3
	s_or_b32 s84, s82, 1
	s_sub_i32 s83, 0xff, s82
	s_sub_i32 s85, 0xff, s84
	s_lshl_b32 s86, s71, 8
	s_cmp_gt_i32 s71, 0
	s_waitcnt lgkmcnt(0)
	s_cselect_b64 s[42:43], -1, 0
	s_cmp_gt_i32 s71, 1
	s_cselect_b64 s[44:45], -1, 0
	s_cmp_gt_i32 s71, 2
	s_waitcnt vmcnt(0)
	v_ashrrev_i32_e32 v17, 3, v126
	s_cselect_b64 s[46:47], -1, 0
	s_cmp_gt_i32 s71, 3
	v_and_b32_e32 v86, 0x7f, v126
	v_and_b32_e32 v87, -16, v17
	v_lshl_add_u32 v91, v127, 2, 0
	v_lshlrev_b32_e32 v3, 1, v127
	s_cselect_b64 s[48:49], -1, 0
	s_cmp_gt_i32 s71, 4
	v_and_b32_e32 v1, 15, v126
	v_lshrrev_b32_e32 v2, 4, v127
	v_sub_u32_e32 v92, v91, v3
	v_mul_u32_u24_e32 v3, 0x90, v86
	v_lshlrev_b32_e32 v4, 1, v87
	s_cselect_b64 s[50:51], -1, 0
	s_cmp_gt_i32 s71, 5
	s_movk_i32 s0, 0x8e
	v_add3_u32 v94, 0, v3, v4
	v_lshlrev_b32_e32 v4, 3, v2
	v_lshlrev_b32_e32 v2, 2, v2
	v_lshlrev_b32_e32 v6, 4, v126
	v_mul_u32_u24_e32 v100, 0x90, v1
	s_cselect_b64 s[52:53], -1, 0
	s_cmp_gt_i32 s71, 6
	v_mad_u32_u24 v93, v127, s0, v92
	v_sub_u32_e32 v2, v1, v2
	v_and_b32_e32 v76, 0x70, v6
	s_movk_i32 s0, 0x110
	v_add3_u32 v101, 0, v100, v4
	s_cselect_b64 s[54:55], -1, 0
	s_cmp_gt_i32 s71, 7
	v_and_b32_e32 v5, 48, v127
	v_mul_lo_u32 v6, v17, s0
	v_lshlrev_b32_e32 v7, 1, v76
	v_cmp_gt_i32_e32 vcc, 0, v2
	v_cmp_gt_i32_e64 s[58:59], 1, v2
	v_cmp_gt_i32_e64 s[62:63], 2, v2
	v_cmp_gt_i32_e64 s[40:41], 3, v2
	v_lshlrev_b32_e32 v2, 7, v1
	v_add_u32_e32 v103, 0x1200, v101
	s_movk_i32 s0, 0x1000
	s_cselect_b64 s[56:57], -1, 0
	s_lshl_b32 s87, s71, 4
	v_add_u32_e32 v95, 0, v5
	v_add3_u32 v96, 0, v6, v7
	v_mul_u32_u24_e32 v6, 0x48, v1
	v_add_u32_e32 v102, 0x900, v101
	v_add3_u32 v8, v103, v2, s0
	v_add_u32_e32 v104, 0x1b00, v101
	s_movk_i32 s0, 0x1800
	s_cmp_lt_u32 s16, 64
	v_lshl_add_u32 v97, v6, 1, v95
	v_add_u32_e32 v6, v101, v2
	v_add3_u32 v7, v102, v2, s1
	v_add3_u32 v2, v104, v2, s0
	s_cselect_b64 s[18:19], -1, 0
	v_or_b32_e32 v1, s87, v1
	s_movk_i32 s0, 0x90
	s_and_b64 s[62:63], s[40:41], s[62:63]
	v_or_b32_e32 v89, 1, v87
	v_mul_i32_i24_e32 v3, 0xffffff74, v127
	v_and_b32_e32 v5, 48, v126
	v_mul_lo_u32 v105, v1, s0
	s_lshl_b32 s0, s71, 5
	s_and_b64 s[72:73], s[62:63], s[58:59]
	v_sub_u32_e32 v88, 0xff, v87
	v_sub_u32_e32 v90, 0xff, v89
	v_mov_b32_e32 v77, v34
	v_add_u32_e32 v98, 0x1200, v97
	v_add_u32_e32 v99, 0x1b00, v97
	v_add3_u32 v106, 0, v105, v4
	v_sub_u32_e32 v107, 0, v17
	v_mov_b32_e32 v178, 0
	v_mov_b32_e32 v179, 0
	v_mov_b32_e32 v180, 0
	v_mov_b32_e32 v181, 0
	v_mov_b32_e32 v182, 0
	v_mov_b32_e32 v183, 0
	v_mov_b32_e32 v184, 0
	v_mov_b32_e32 v185, 0
	v_mov_b32_e32 v186, 0
	v_mov_b32_e32 v187, 0
	v_mov_b32_e32 v188, 0
	v_mov_b32_e32 v189, 0
	v_mov_b32_e32 v190, 0
	v_mov_b32_e32 v192, 0
	v_mov_b32_e32 v194, 0
	v_mov_b32_e32 v196, 0
	v_mov_b32_e32 v200, 0
	v_mov_b32_e32 v201, 0
	v_mov_b32_e32 v202, 0
	v_mov_b32_e32 v203, 0
	v_mov_b32_e32 v206, 0
	v_mov_b32_e32 v207, 0
	v_mov_b32_e32 v208, 0
	v_mov_b32_e32 v209, 0
	v_lshrrev_b32_e32 v218, 4, v127
	v_lshl_add_u32 v218, v218, 2, s87
	s_sub_i32 s16, 0, s82
	v_sub_u32_e32 v108, 0, v87
	v_add_u32_e32 v109, v93, v3
	v_add_u32_e32 v110, s0, v6
	v_add_u32_e32 v111, s0, v7
	v_add_u32_e32 v112, s0, v8
	v_add_u32_e32 v113, s0, v2
	v_add_u32_e32 v114, 0, v5
	s_and_b64 s[2:3], s[72:73], vcc
	s_mov_b32 s17, s20
	s_cmp_ge_u32 s71, 4
	s_cbranch_scc0 .Lprio_gla
	s_setprio 1

.LBB0_467:
	v_mov_b32_e32 v115, 0
	v_mov_b32_e32 v116, 0
	v_mov_b32_e32 v117, 0
	v_mov_b32_e32 v118, 0
	v_mov_b32_e32 v119, 0
	v_mov_b32_e32 v120, 0
	v_mov_b32_e32 v121, 0
	v_mov_b32_e32 v122, 0
	v_mov_b32_e32 v123, 0
	v_mov_b32_e32 v124, 0
	v_mov_b32_e32 v125, 0
	v_mov_b32_e32 v128, 0
	v_mov_b32_e32 v129, 0
	v_mov_b32_e32 v130, 0
	v_mov_b32_e32 v131, 0
	v_mov_b32_e32 v132, 0
	v_mov_b32_e32 v133, 0
	v_mov_b32_e32 v134, 0
	v_mov_b32_e32 v135, 0
	v_mov_b32_e32 v136, 0
	v_mov_b32_e32 v137, 0
	v_mov_b32_e32 v138, 0
	v_mov_b32_e32 v139, 0
	v_mov_b32_e32 v140, 0
	s_bfe_u32 s0, s17, 0x50002
	s_and_b32 s36, s17, 3
	s_lshl_b32 s1, s17, 1
	s_and_b32 s37, s1, 0x7fffff00
	s_lshl_b32 s1, s36, 7
	s_lshl_b32 s88, s0, 8
	s_cmpk_lt_u32 s17, 0x80
	s_cselect_b64 s[58:59], -1, 0
	s_and_b64 s[14:15], s[58:59], exec
	v_lshl_or_b32 v2, s36, 6, v127
	s_mov_b32 s14, 0x38600000
	v_lshlrev_b32_e32 v78, 1, v2
	v_or_b32_e32 v2, s37, v2
	s_cselect_b32 s15, s82, s83
	s_cselect_b32 s37, s84, s85
	s_cselect_b32 s14, s14, 0x3ce00000
	s_add_i32 s36, s88, s15
	s_add_i32 s64, s88, s37
	s_sub_i32 s94, s64, s36
	s_ashr_i32 s37, s36, 31
	s_mul_i32 s90, s36, 0x1800
	s_mul_hi_i32 s65, s36, 0x1800
	s_add_u32 s90, s90, s80
	s_addc_u32 s91, s65, s81
	s_lshl_b64 s[92:93], s[36:37], 10
	s_add_u32 s92, s92, s78
	s_addc_u32 s93, s93, s79
	v_lshlrev_b32_e32 v80, 1, v2
	global_load_short_d16_hi v115, v78, s[90:91]
	global_load_short_d16_hi v116, v78, s[90:91] offset:512
	global_load_short_d16_hi v117, v80, s[92:93]
	s_ashr_i32 s65, s64, 31
	s_mul_i32 s90, s64, 0x1800
	s_mul_hi_i32 s37, s64, 0x1800
	s_add_u32 s90, s90, s80
	s_addc_u32 s91, s37, s81
	s_lshl_b64 s[64:65], s[64:65], 10
	s_add_u32 s64, s64, s78
	s_addc_u32 s65, s65, s79
	s_lshl_b32 s37, s94, 1
	s_add_i32 s36, s37, s36
	global_load_short_d16_hi v118, v78, s[90:91]
	global_load_short_d16_hi v119, v78, s[90:91] offset:512
	global_load_short_d16_hi v120, v80, s[64:65]
	s_ashr_i32 s37, s36, 31
	s_mul_i32 s64, s36, 0x1800
	s_mul_hi_i32 s65, s36, 0x1800
	s_add_u32 s64, s64, s80
	s_addc_u32 s65, s65, s81
	s_lshl_b64 s[90:91], s[36:37], 10
	s_add_u32 s90, s90, s78
	s_addc_u32 s91, s91, s79
	s_add_i32 s36, s36, s94
	global_load_short_d16_hi v121, v78, s[64:65]
	global_load_short_d16_hi v122, v78, s[64:65] offset:512
	global_load_short_d16_hi v123, v80, s[90:91]
	s_ashr_i32 s37, s36, 31
	s_mul_i32 s64, s36, 0x1800
	s_mul_hi_i32 s65, s36, 0x1800
	s_add_u32 s64, s64, s80
	s_addc_u32 s65, s65, s81
	s_lshl_b64 s[90:91], s[36:37], 10
	s_add_u32 s90, s90, s78
	s_addc_u32 s91, s91, s79
	s_add_i32 s36, s36, s94
	global_load_short_d16_hi v124, v78, s[64:65]
	global_load_short_d16_hi v125, v78, s[64:65] offset:512
	global_load_short_d16_hi v128, v80, s[90:91]
	s_ashr_i32 s37, s36, 31
	s_mul_i32 s64, s36, 0x1800
	s_mul_hi_i32 s65, s36, 0x1800
	s_add_u32 s64, s64, s80
	s_addc_u32 s65, s65, s81
	s_lshl_b64 s[90:91], s[36:37], 10
	s_add_u32 s90, s90, s78
	s_addc_u32 s91, s91, s79
	s_add_i32 s36, s36, s94
	global_load_short_d16_hi v129, v78, s[64:65]
	global_load_short_d16_hi v130, v78, s[64:65] offset:512
	global_load_short_d16_hi v131, v80, s[90:91]
	s_ashr_i32 s37, s36, 31
	s_mul_i32 s64, s36, 0x1800
	s_mul_hi_i32 s65, s36, 0x1800
	s_add_u32 s64, s64, s80
	s_addc_u32 s65, s65, s81
	s_lshl_b64 s[90:91], s[36:37], 10
	s_add_u32 s90, s90, s78
	s_addc_u32 s91, s91, s79
	s_add_i32 s36, s36, s94
	global_load_short_d16_hi v132, v78, s[64:65]
	global_load_short_d16_hi v133, v78, s[64:65] offset:512
	global_load_short_d16_hi v134, v80, s[90:91]
	s_ashr_i32 s37, s36, 31
	s_mul_i32 s64, s36, 0x1800
	s_mul_hi_i32 s65, s36, 0x1800
	s_add_u32 s64, s64, s80
	s_addc_u32 s65, s65, s81
	s_lshl_b64 s[90:91], s[36:37], 10
	s_add_u32 s90, s90, s78
	s_addc_u32 s91, s91, s79
	s_add_i32 s36, s36, s94
	global_load_short_d16_hi v135, v78, s[64:65]
	global_load_short_d16_hi v136, v78, s[64:65] offset:512
	global_load_short_d16_hi v137, v80, s[90:91]
	s_ashr_i32 s37, s36, 31
	s_mul_i32 s64, s36, 0x1800
	s_mul_hi_i32 s65, s36, 0x1800
	s_add_u32 s64, s64, s80
	s_addc_u32 s65, s65, s81
	s_lshl_b64 s[36:37], s[36:37], 10
	s_add_u32 s36, s36, s78
	v_cndmask_b32_e64 v1, v88, v87, s[58:59]
	v_cndmask_b32_e64 v3, v90, v89, s[58:59]
	s_addc_u32 s37, s37, s79
	v_add_u32_e32 v1, s88, v1
	v_add_u32_e32 v3, s88, v3
	global_load_short_d16_hi v138, v78, s[64:65]
	global_load_short_d16_hi v139, v78, s[64:65] offset:512
	global_load_short_d16_hi v140, v80, s[36:37]
	v_readfirstlane_b32 s15, v3
	v_readfirstlane_b32 s64, v1
	s_sub_i32 s90, s15, s64
	s_mul_i32 s36, s64, 0x1800
	s_mul_hi_i32 s37, s64, 0x1800
	s_add_u32 s36, s36, s80
	v_or_b32_e32 v2, s1, v86
	s_addc_u32 s37, s37, s81
	v_lshl_or_b32 v82, v2, 1, v239
	global_load_ushort v2, v82, s[36:37]
	s_mul_hi_i32 s37, s15, 0x1800
	s_mulk_i32 s15, 0x1800
	s_add_u32 s36, s15, s80
	s_addc_u32 s37, s37, s81
	s_lshl_b32 s15, s90, 1
	s_add_i32 s15, s15, s64
	global_load_ushort v1, v82, s[36:37]
	s_mul_i32 s36, s15, 0x1800
	s_mul_hi_i32 s37, s15, 0x1800
	s_add_u32 s36, s36, s80
	s_addc_u32 s37, s37, s81
	s_add_i32 s15, s15, s90
	global_load_ushort v4, v82, s[36:37]
	s_mul_i32 s36, s15, 0x1800
	s_mul_hi_i32 s37, s15, 0x1800
	s_add_u32 s36, s36, s80
	s_addc_u32 s37, s37, s81
	s_add_i32 s15, s15, s90
	global_load_ushort v3, v82, s[36:37]
	s_mul_i32 s36, s15, 0x1800
	s_mul_hi_i32 s37, s15, 0x1800
	s_add_u32 s36, s36, s80
	s_addc_u32 s37, s37, s81
	s_add_i32 s15, s15, s90
	global_load_ushort v6, v82, s[36:37]
	s_mul_i32 s36, s15, 0x1800
	s_mul_hi_i32 s37, s15, 0x1800
	s_add_u32 s36, s36, s80
	s_addc_u32 s37, s37, s81
	s_add_i32 s15, s15, s90
	global_load_ushort v5, v82, s[36:37]
	s_mul_i32 s36, s15, 0x1800
	s_mul_hi_i32 s37, s15, 0x1800
	s_add_u32 s36, s36, s80
	s_addc_u32 s37, s37, s81
	s_add_i32 s15, s15, s90
	global_load_ushort v8, v82, s[36:37]
	s_mul_i32 s36, s15, 0x1800
	s_mul_hi_i32 s37, s15, 0x1800
	s_add_u32 s36, s36, s80
	s_addc_u32 s37, s37, s81
	s_add_i32 s15, s15, s90
	global_load_ushort v7, v82, s[36:37]
	s_mul_i32 s36, s15, 0x1800
	s_mul_hi_i32 s37, s15, 0x1800
	s_add_u32 s36, s36, s80
	s_addc_u32 s37, s37, s81
	s_add_i32 s15, s15, s90
	global_load_ushort v10, v82, s[36:37]
	s_mul_i32 s36, s15, 0x1800
	s_mul_hi_i32 s37, s15, 0x1800
	s_add_u32 s36, s36, s80
	s_addc_u32 s37, s37, s81
	s_add_i32 s15, s15, s90
	global_load_ushort v9, v82, s[36:37]
	s_mul_i32 s36, s15, 0x1800
	s_mul_hi_i32 s37, s15, 0x1800
	s_add_u32 s36, s36, s80
	s_addc_u32 s37, s37, s81
	s_add_i32 s15, s15, s90
	global_load_ushort v12, v82, s[36:37]
	s_mul_i32 s36, s15, 0x1800
	s_mul_hi_i32 s37, s15, 0x1800
	s_add_u32 s36, s36, s80
	s_addc_u32 s37, s37, s81
	s_add_i32 s15, s15, s90
	global_load_ushort v11, v82, s[36:37]
	s_mul_i32 s36, s15, 0x1800
	s_mul_hi_i32 s37, s15, 0x1800
	s_add_u32 s36, s36, s80
	s_addc_u32 s37, s37, s81
	s_add_i32 s15, s15, s90
	s_mul_i32 s64, s15, 0x1800
	s_mul_hi_i32 s65, s15, 0x1800
	s_add_u32 s64, s64, s80
	s_addc_u32 s65, s65, s81
	s_add_i32 s15, s15, s90
	global_load_ushort v14, v82, s[36:37]
	s_mul_i32 s36, s15, 0x1800
	s_mul_hi_i32 s37, s15, 0x1800
	s_add_u32 s36, s36, s80
	s_addc_u32 s37, s37, s81
	s_add_i32 s15, s15, s90
	global_load_ushort v13, v82, s[64:65]
	s_mul_hi_i32 s65, s15, 0x1800
	s_mulk_i32 s15, 0x1800
	s_add_u32 s64, s15, s80
	s_addc_u32 s65, s65, s81
	global_load_ushort v16, v82, s[36:37]
	global_load_ushort v15, v82, s[64:65]
	s_add_u32 s14, s76, s14
	s_addc_u32 s15, s77, 0
	s_lshl_b32 s90, s0, 11
	s_addk_i32 s90, 0x2000
	s_add_u32 s0, s14, s1
	s_addc_u32 s1, s15, 0
	s_waitcnt vmcnt(0)
	v_mov_b32_e32 v18, 0
	s_mov_b32 s89, 0
	v_mov_b32_e32 v79, v34
	v_mov_b32_e32 v81, v34
	v_mov_b32_e32 v83, v34
	s_mov_b32 s91, 0
	s_mov_b32 s92, 0
	v_mov_b32_e32 v19, v18
	v_mov_b32_e32 v20, v18
	v_mov_b32_e32 v21, v18
	v_mov_b32_e32 v22, v18
	v_mov_b32_e32 v23, v18
	v_mov_b32_e32 v24, v18
	v_mov_b32_e32 v25, v18
	v_mov_b32_e32 v26, v18
	v_mov_b32_e32 v27, v18
	v_mov_b32_e32 v28, v18
	v_mov_b32_e32 v29, v18
	v_mov_b32_e32 v36, v18
	v_mov_b32_e32 v37, v18
	v_mov_b32_e32 v38, v18
	v_mov_b32_e32 v39, v18
	v_lshl_add_u64 v[84:85], s[0:1], 0, v[76:77]
	s_mov_b64 s[94:95], s[0:1]
	s_barrier
	s_branch .LBB0_469

.Lgp_skip:
	v_add_f32_e32 v32, 0, v117
	v_add_u32_e32 v210, s98, v210
	global_load_short_d16_hi v178, v210, s[80:81]
	v_add_f32_e32 v40, v32, v120
	v_add_f32_e32 v41, v40, v123
	global_load_short_d16_hi v179, v210, s[80:81] offset:512
	v_add_f32_e32 v42, v41, v128
	v_add_f32_e32 v43, v42, v131
	v_add_f32_e32 v44, v43, v134
	v_add_u32_e32 v211, s99, v211
	global_load_short_d16_hi v180, v211, s[78:79]
	v_add_f32_e32 v45, v44, v137
	v_add_f32_e32 v33, v45, v140
	v_add_u32_e32 v30, s86, v91
	v_add_u32_e32 v210, s98, v210
	global_load_short_d16_hi v181, v210, s[80:81]
	ds_write_b32 v30, v33 offset:46080
	s_waitcnt lgkmcnt(0)
	s_barrier
	ds_read2st64_b32 v[30:31], v91 offset0:180 offset1:181
	ds_read2st64_b32 v[248:249], v91 offset0:182 offset1:183
	ds_read2st64_b32 v[250:251], v91 offset0:184 offset1:185
	ds_read2st64_b32 v[252:253], v91 offset0:186 offset1:187
	global_load_short_d16_hi v182, v210, s[80:81] offset:512
	v_mul_f32_e32 v47, 0x3e000000, v115
	s_andn2_b64 vcc, exec, s[18:19]
	s_waitcnt lgkmcnt(0)
	v_add_f32_e32 v30, 0, v30
	v_cndmask_b32_e64 v35, 0, v30, s[42:43]
	v_add_u32_e32 v211, s99, v211
	global_load_short_d16_hi v183, v211, s[78:79]
	v_add_f32_e32 v46, v30, v31
	v_add_f32_e32 v30, v31, v35
	v_cndmask_b32_e64 v35, v35, v30, s[44:45]
	v_add_u32_e32 v210, s98, v210
	global_load_short_d16_hi v184, v210, s[80:81]
	v_add_f32_e32 v46, v46, v248
	v_add_f32_e32 v30, v248, v35
	v_cndmask_b32_e64 v30, v35, v30, s[46:47]
	v_add_f32_e32 v35, v46, v249
	v_add_f32_e32 v31, v249, v30
	global_load_short_d16_hi v185, v210, s[80:81] offset:512
	v_cndmask_b32_e64 v46, v30, v31, s[48:49]
	v_add_f32_e32 v35, v35, v250
	v_add_f32_e32 v30, v250, v46
	v_add_u32_e32 v211, s99, v211
	global_load_short_d16_hi v186, v211, s[78:79]
	v_cndmask_b32_e64 v30, v46, v30, s[50:51]
	v_add_f32_e32 v35, v35, v251
	v_add_f32_e32 v31, v251, v30
	v_cndmask_b32_e64 v46, v30, v31, s[52:53]
	v_add_u32_e32 v210, s98, v210
	global_load_short_d16_hi v187, v210, s[80:81]
	v_add_f32_e32 v35, v35, v252
	v_add_f32_e32 v30, v252, v46
	v_cndmask_b32_e64 v30, v46, v30, s[54:55]
	v_add_f32_e32 v35, v35, v253
	v_add_f32_e32 v31, v253, v30
	global_load_short_d16_hi v188, v210, s[80:81] offset:512
	v_cndmask_b32_e64 v46, v30, v31, s[56:57]
	v_mul_f32_e32 v30, 0x3fb8aa3b, v35
	v_exp_f32_e32 v35, v30
	v_add_f32_e32 v30, v32, v46
	v_mul_f32_e32 v30, 0x3fb8aa3b, v30
	v_add_u32_e32 v211, s99, v211
	global_load_short_d16_hi v189, v211, s[78:79]
	v_exp_f32_e32 v30, v30
	v_add_f32_e32 v33, v33, v46
	v_mul_f32_e32 v33, 0x3fb8aa3b, v33
	v_exp_f32_e32 v33, v33
	v_rcp_f32_e32 v31, v30
	v_add_u32_e32 v210, s98, v210
	global_load_short_d16_hi v190, v210, s[80:81]
	v_mul_f32_e32 v30, v47, v30
	v_cvt_pk_bf16_f32 v30, v30, s0
	s_mul_i32 s0, s71, 0x480
	v_add_u32_e32 v47, s0, v92
	v_mul_f32_e32 v32, v35, v31
	global_load_short_d16_hi v192, v210, s[80:81] offset:512
	ds_write_b16 v47, v30
	v_mul_f32_e32 v30, v31, v116
	v_add_f32_e32 v31, v40, v46
	v_mul_f32_e32 v31, 0x3fb8aa3b, v31
	v_exp_f32_e32 v31, v31
	v_add_u32_e32 v211, s99, v211
	global_load_short_d16_hi v194, v211, s[78:79]
	v_cvt_pk_bf16_f32 v30, v30, s0
	ds_write_b16 v47, v30 offset:9216
	v_mul_f32_e32 v30, v32, v116
	v_rcp_f32_e32 v32, v31
	v_add_u32_e32 v210, s98, v210
	global_load_short_d16_hi v196, v210, s[80:81]
	v_mul_f32_e32 v40, 0x3e000000, v118
	v_mul_f32_e32 v31, v40, v31
	v_cvt_pk_bf16_f32 v31, v31, s0
	ds_write_b16 v47, v31 offset:144
	global_load_short_d16_hi v200, v210, s[80:81] offset:512
	v_mul_f32_e32 v31, v32, v119
	v_cvt_pk_bf16_f32 v31, v31, s0
	ds_write_b16 v47, v31 offset:9360
	v_mul_f32_e32 v31, v35, v32
	v_mul_f32_e32 v31, v31, v119
	v_add_u32_e32 v211, s99, v211
	global_load_short_d16_hi v201, v211, s[78:79]
	v_cvt_pk_bf16_f32 v31, v31, 0
	v_cvt_pk_bf16_f32 v30, v30, 0
	v_lshlrev_b32_e32 v31, 16, v31
	v_and_or_b32 v30, v30, s27, v31
	v_add_f32_e32 v31, v41, v46
	v_add_u32_e32 v210, s98, v210
	global_load_short_d16_hi v202, v210, s[80:81]
	v_mul_f32_e32 v31, 0x3fb8aa3b, v31
	v_exp_f32_e32 v31, v31
	v_mul_f32_e32 v41, 0x3e000000, v121
	global_load_short_d16_hi v203, v210, s[80:81] offset:512
	v_rcp_f32_e32 v32, v31
	v_mul_f32_e32 v31, v41, v31
	v_cvt_pk_bf16_f32 v31, v31, s0
	ds_write_b16 v47, v31 offset:288
	v_mul_f32_e32 v40, v35, v32
	v_add_u32_e32 v211, s99, v211
	global_load_short_d16_hi v206, v211, s[78:79]
	v_mul_f32_e32 v31, v32, v122
	v_add_f32_e32 v32, v42, v46
	v_mul_f32_e32 v32, 0x3fb8aa3b, v32
	v_exp_f32_e32 v32, v32
	v_cvt_pk_bf16_f32 v31, v31, s0
	v_add_u32_e32 v210, s98, v210
	global_load_short_d16_hi v207, v210, s[80:81]
	ds_write_b16 v47, v31 offset:9504
	v_mul_f32_e32 v31, v40, v122
	v_rcp_f32_e32 v40, v32
	v_mul_f32_e32 v41, 0x3e000000, v124
	global_load_short_d16_hi v208, v210, s[80:81] offset:512
	v_mul_f32_e32 v32, v41, v32
	v_cvt_pk_bf16_f32 v32, v32, s0
	ds_write_b16 v47, v32 offset:432
	v_mul_f32_e32 v32, v40, v125
	v_add_u32_e32 v211, s99, v211
	global_load_short_d16_hi v209, v211, s[78:79]
	v_cvt_pk_bf16_f32 v32, v32, s0
	ds_write_b16 v47, v32 offset:9648
	v_mul_f32_e32 v32, v35, v40
	v_mul_f32_e32 v32, v32, v125
	v_cvt_pk_bf16_f32 v32, v32, 0
	v_add_u32_e32 v214, s100, v214
	global_load_ushort v220, v214, s[80:81]
	v_cvt_pk_bf16_f32 v31, v31, 0
	v_lshlrev_b32_e32 v32, 16, v32
	v_and_or_b32 v31, v31, s27, v32
	v_add_f32_e32 v32, v43, v46
	v_mul_f32_e32 v32, 0x3fb8aa3b, v32
	v_add_u32_e32 v214, s100, v214
	global_load_ushort v219, v214, s[80:81]
	v_exp_f32_e32 v32, v32
	v_mul_f32_e32 v42, 0x3e000000, v129
	v_rcp_f32_e32 v40, v32
	v_add_u32_e32 v214, s100, v214
	global_load_ushort v222, v214, s[80:81]
	v_mul_f32_e32 v32, v42, v32
	v_cvt_pk_bf16_f32 v32, v32, s0
	ds_write_b16 v47, v32 offset:576
	v_mul_f32_e32 v41, v35, v40
	v_mul_f32_e32 v32, v40, v130
	v_add_u32_e32 v214, s100, v214
	global_load_ushort v221, v214, s[80:81]
	v_add_f32_e32 v40, v44, v46
	v_mul_f32_e32 v40, 0x3fb8aa3b, v40
	v_exp_f32_e32 v40, v40
	v_cvt_pk_bf16_f32 v32, v32, s0
	ds_write_b16 v47, v32 offset:9792
	v_add_u32_e32 v214, s100, v214
	global_load_ushort v224, v214, s[80:81]
	v_mul_f32_e32 v32, v41, v130
	v_rcp_f32_e32 v41, v40
	v_mul_f32_e32 v42, 0x3e000000, v132
	v_mul_f32_e32 v40, v42, v40
	v_add_u32_e32 v214, s100, v214
	global_load_ushort v223, v214, s[80:81]
	v_cvt_pk_bf16_f32 v40, v40, s0
	ds_write_b16 v47, v40 offset:720
	v_mul_f32_e32 v40, v41, v133
	v_cvt_pk_bf16_f32 v40, v40, s0
	ds_write_b16 v47, v40 offset:9936
	v_add_u32_e32 v214, s100, v214
	global_load_ushort v226, v214, s[80:81]
	v_mul_f32_e32 v40, v35, v41
	v_mul_f32_e32 v40, v40, v133
	v_cvt_pk_bf16_f32 v40, v40, 0
	v_cvt_pk_bf16_f32 v32, v32, 0
	v_lshlrev_b32_e32 v40, 16, v40
	v_add_u32_e32 v214, s100, v214
	global_load_ushort v225, v214, s[80:81]
	v_and_or_b32 v32, v32, s27, v40
	v_add_f32_e32 v40, v45, v46
	v_mul_f32_e32 v40, 0x3fb8aa3b, v40
	v_exp_f32_e32 v40, v40
	v_add_u32_e32 v214, s100, v214
	global_load_ushort v228, v214, s[80:81]
	v_mul_f32_e32 v43, 0x3e000000, v135
	v_rcp_f32_e32 v41, v40
	v_mul_f32_e32 v40, v43, v40
	v_cvt_pk_bf16_f32 v40, v40, s0
	v_add_u32_e32 v214, s100, v214
	global_load_ushort v227, v214, s[80:81]
	ds_write_b16 v47, v40 offset:864
	v_mul_f32_e32 v40, v41, v136
	v_mul_f32_e32 v42, v35, v41
	v_cvt_pk_bf16_f32 v40, v40, s0
	ds_write_b16 v47, v40 offset:10080
	v_add_u32_e32 v214, s100, v214
	global_load_ushort v230, v214, s[80:81]
	v_mul_f32_e32 v40, v42, v136
	v_rcp_f32_e32 v41, v33
	v_mul_f32_e32 v42, 0x3e000000, v138
	v_mul_f32_e32 v33, v42, v33
	v_add_u32_e32 v214, s100, v214
	global_load_ushort v229, v214, s[80:81]
	v_cvt_pk_bf16_f32 v33, v33, s0
	ds_write_b16 v47, v33 offset:1008
	v_mul_f32_e32 v33, v41, v139
	v_cvt_pk_bf16_f32 v33, v33, s0
	v_add_u32_e32 v214, s100, v214
	global_load_ushort v232, v214, s[80:81]
	ds_write_b16 v47, v33 offset:10224
	v_mul_f32_e32 v33, v35, v41
	v_mul_f32_e32 v33, v33, v139
	v_cvt_pk_bf16_f32 v33, v33, 0
	v_cvt_pk_bf16_f32 v40, v40, 0
	v_add_u32_e32 v214, s100, v214
	global_load_ushort v231, v214, s[80:81]
	v_lshlrev_b32_e32 v33, 16, v33
	v_and_or_b32 v33, v40, s27, v33
	v_add_u32_e32 v40, s87, v93
	ds_write_b128 v40, v[30:33] offset:18432
	s_cbranch_vccnz .LBB0_471
	ds_write_b32 v109, v35 offset:48128
